# MoE tile table: the 32-step prefix sum by thread 0 reads all expert counts at once (8 ds_read_b128) instead of 32 dependent LDS write/read round trips
# speedup vs baseline: 1.0144x; 1.0029x over previous
; #define LAS __attribute__((address_space(3)))
; __global__ void __launch_bounds__(512, 2) fwd_kernel(Args args) {
;     ...
;         volatile LAS int* tbw = (volatile LAS int*)(F.MISC + 16); volatile LAS int* cntw = (volatile LAS int*)(F.MISC + 128);
;         if (F.tid < 32) cntw[F.tid] = (int)__hip_atomic_load(F.ctl + CW_CNT + (l * NE + F.tid) * 64, __ATOMIC_RELAXED, __HIP_MEMORY_SCOPE_AGENT);
;         __syncthreads();
;         if (F.tid == 0) { int s = 0; for (int e = 0; e < NE; ++e) { tbw[e] = s; s += (cntw[e] + 255) >> 8; } tbw[32] = s; }
;         __syncthreads();
.LBB0_1174:
	s_or_b64 exec, exec, s[2:3]
	s_waitcnt lgkmcnt(0)
	s_barrier
	s_and_saveexec_b64 s[6:7], s[4:5]
	s_cbranch_execz .LBB0_1176
	v_mov_b32_e32 v100, 0x20200
	ds_read_b128 v[104:107], v100
	ds_read_b128 v[108:111], v100 offset:16
	ds_read_b128 v[112:115], v100 offset:32
	ds_read_b128 v[116:119], v100 offset:48
	ds_read_b128 v[120:123], v100 offset:64
	ds_read_b128 v[124:127], v100 offset:80
	ds_read_b128 v[128:131], v100 offset:96
	ds_read_b128 v[132:135], v100 offset:112
	v_mov_b32_e32 v101, 0x20040
	v_mov_b32_e32 v102, 0
	s_waitcnt lgkmcnt(0)
	ds_write_b32 v101, v102
	v_add_u32_e32 v104, 0xff, v104
	v_ashrrev_i32_e32 v104, 8, v104
	v_add_u32_e32 v102, v102, v104
	ds_write_b32 v101, v102 offset:4
	v_add_u32_e32 v105, 0xff, v105
	v_ashrrev_i32_e32 v105, 8, v105
	v_add_u32_e32 v102, v102, v105
	ds_write_b32 v101, v102 offset:8
	v_add_u32_e32 v106, 0xff, v106
	v_ashrrev_i32_e32 v106, 8, v106
	v_add_u32_e32 v102, v102, v106
	ds_write_b32 v101, v102 offset:12
	v_add_u32_e32 v107, 0xff, v107
	v_ashrrev_i32_e32 v107, 8, v107
	v_add_u32_e32 v102, v102, v107
	ds_write_b32 v101, v102 offset:16
	v_add_u32_e32 v108, 0xff, v108
	v_ashrrev_i32_e32 v108, 8, v108
	v_add_u32_e32 v102, v102, v108
	ds_write_b32 v101, v102 offset:20
	v_add_u32_e32 v109, 0xff, v109
	v_ashrrev_i32_e32 v109, 8, v109
	v_add_u32_e32 v102, v102, v109
	ds_write_b32 v101, v102 offset:24
	v_add_u32_e32 v110, 0xff, v110
	v_ashrrev_i32_e32 v110, 8, v110
	v_add_u32_e32 v102, v102, v110
	ds_write_b32 v101, v102 offset:28
	v_add_u32_e32 v111, 0xff, v111
	v_ashrrev_i32_e32 v111, 8, v111
	v_add_u32_e32 v102, v102, v111
	ds_write_b32 v101, v102 offset:32
	v_add_u32_e32 v112, 0xff, v112
	v_ashrrev_i32_e32 v112, 8, v112
	v_add_u32_e32 v102, v102, v112
	ds_write_b32 v101, v102 offset:36
	v_add_u32_e32 v113, 0xff, v113
	v_ashrrev_i32_e32 v113, 8, v113
	v_add_u32_e32 v102, v102, v113
	ds_write_b32 v101, v102 offset:40
	v_add_u32_e32 v114, 0xff, v114
	v_ashrrev_i32_e32 v114, 8, v114
	v_add_u32_e32 v102, v102, v114
	ds_write_b32 v101, v102 offset:44
	v_add_u32_e32 v115, 0xff, v115
	v_ashrrev_i32_e32 v115, 8, v115
	v_add_u32_e32 v102, v102, v115
	ds_write_b32 v101, v102 offset:48
	v_add_u32_e32 v116, 0xff, v116
	v_ashrrev_i32_e32 v116, 8, v116
	v_add_u32_e32 v102, v102, v116
	ds_write_b32 v101, v102 offset:52
	v_add_u32_e32 v117, 0xff, v117
	v_ashrrev_i32_e32 v117, 8, v117
	v_add_u32_e32 v102, v102, v117
	ds_write_b32 v101, v102 offset:56
	v_add_u32_e32 v118, 0xff, v118
	v_ashrrev_i32_e32 v118, 8, v118
	v_add_u32_e32 v102, v102, v118
	ds_write_b32 v101, v102 offset:60
	v_add_u32_e32 v119, 0xff, v119
	v_ashrrev_i32_e32 v119, 8, v119
	v_add_u32_e32 v102, v102, v119
	ds_write_b32 v101, v102 offset:64
	v_add_u32_e32 v120, 0xff, v120
	v_ashrrev_i32_e32 v120, 8, v120
	v_add_u32_e32 v102, v102, v120
	ds_write_b32 v101, v102 offset:68
	v_add_u32_e32 v121, 0xff, v121
	v_ashrrev_i32_e32 v121, 8, v121
	v_add_u32_e32 v102, v102, v121
	ds_write_b32 v101, v102 offset:72
	v_add_u32_e32 v122, 0xff, v122
	v_ashrrev_i32_e32 v122, 8, v122
	v_add_u32_e32 v102, v102, v122
	ds_write_b32 v101, v102 offset:76
	v_add_u32_e32 v123, 0xff, v123
	v_ashrrev_i32_e32 v123, 8, v123
	v_add_u32_e32 v102, v102, v123
	ds_write_b32 v101, v102 offset:80
	v_add_u32_e32 v124, 0xff, v124
	v_ashrrev_i32_e32 v124, 8, v124
	v_add_u32_e32 v102, v102, v124
	ds_write_b32 v101, v102 offset:84
	v_add_u32_e32 v125, 0xff, v125
	v_ashrrev_i32_e32 v125, 8, v125
	v_add_u32_e32 v102, v102, v125
	ds_write_b32 v101, v102 offset:88
	v_add_u32_e32 v126, 0xff, v126
	v_ashrrev_i32_e32 v126, 8, v126
	v_add_u32_e32 v102, v102, v126
	ds_write_b32 v101, v102 offset:92
	v_add_u32_e32 v127, 0xff, v127
	v_ashrrev_i32_e32 v127, 8, v127
	v_add_u32_e32 v102, v102, v127
	ds_write_b32 v101, v102 offset:96
	v_add_u32_e32 v128, 0xff, v128
	v_ashrrev_i32_e32 v128, 8, v128
	v_add_u32_e32 v102, v102, v128
	ds_write_b32 v101, v102 offset:100
	v_add_u32_e32 v129, 0xff, v129
	v_ashrrev_i32_e32 v129, 8, v129
	v_add_u32_e32 v102, v102, v129
	ds_write_b32 v101, v102 offset:104
	v_add_u32_e32 v130, 0xff, v130
	v_ashrrev_i32_e32 v130, 8, v130
	v_add_u32_e32 v102, v102, v130
	ds_write_b32 v101, v102 offset:108
	v_add_u32_e32 v131, 0xff, v131
	v_ashrrev_i32_e32 v131, 8, v131
	v_add_u32_e32 v102, v102, v131
	ds_write_b32 v101, v102 offset:112
	v_add_u32_e32 v132, 0xff, v132
	v_ashrrev_i32_e32 v132, 8, v132
	v_add_u32_e32 v102, v102, v132
	ds_write_b32 v101, v102 offset:116
	v_add_u32_e32 v133, 0xff, v133
	v_ashrrev_i32_e32 v133, 8, v133
	v_add_u32_e32 v102, v102, v133
	ds_write_b32 v101, v102 offset:120
	v_add_u32_e32 v134, 0xff, v134
	v_ashrrev_i32_e32 v134, 8, v134
	v_add_u32_e32 v102, v102, v134
	ds_write_b32 v101, v102 offset:124
	v_add_u32_e32 v135, 0xff, v135
	v_ashrrev_i32_e32 v135, 8, v135
	v_add_u32_e32 v102, v102, v135
	ds_write_b32 v101, v102 offset:128
